# vq_final entropy terms reduced in registers (DPP) with the barrier after the atomic issue; output waves skip store-ack waits at recheck entry
# speedup vs baseline: 1.0356x; 1.0009x over previous
.LBB0_107:
	s_cmp_lt_u32 s33, 4
	s_cbranch_scc1 .Lskipvm
	s_waitcnt vmcnt(0)
.Lskipvm:
	v_lshrrev_b32_e32 v177, 4, v0
	v_and_b32_e32 v166, 63, v0
	s_setprio 0
	v_mov_b32_e32 v66, 0x21d44
	ds_read_b32 v183, v66
	s_mov_b32 s25, 0
	v_mbcnt_lo_u32_b32 v176, -1, 0
	s_waitcnt lgkmcnt(0)
	v_cmp_eq_u32_e32 vcc, 0, v183
	s_cbranch_vccnz .LBB0_455
	v_mov_b32_e32 v169, 0
	v_mov_b32_e32 v179, v169
	v_lshlrev_b32_e32 v67, 2, v184
	v_lshlrev_b32_e32 v68, 10, v181
	v_lshl_add_u64 v[170:171], s[20:21], 0, v[178:179]
	v_mov_b32_e32 v66, 0x21c00
	v_lshl_add_u64 v[172:173], s[12:13], 0, v[178:179]
	v_or3_b32 v179, s3, v67, v68
	v_mov_b32_e32 v246, 0x1c400
	v_mov_b32_e32 v174, -1
	v_cmp_gt_u32_e64 s[4:5], 32, v0
	v_lshl_add_u32 v185, v0, 3, v66
	v_cmp_eq_u32_e64 s[6:7], 0, v1
	v_lshl_or_b32 v184, v177, 3, v66
	v_lshl_or_b32 v247, v177, 2, v246
	v_mov_b32_e32 v248, 0x21d40
	s_movk_i32 s3, 0x90
	s_movk_i32 s20, 0x800
	s_movk_i32 s21, 0x3ff0
	s_movk_i32 s26, 0xfc00
	v_mov_b32_e32 v249, 0x21400
	v_mov_b32_e32 v175, v174
	v_mov_b32_e32 v250, 0x20400
	v_mbcnt_hi_u32_b32 v251, -1, v176
	v_mov_b32_e32 v252, 0x20c00
	s_branch .LBB0_110

.LBB0_110:
	v_add_u32_e32 v66, s25, v177
	v_cmp_lt_u32_e64 s[8:9], v66, v183
	v_mov_b32_e32 v253, v169
	s_and_saveexec_b64 s[0:1], s[8:9]
	v_lshl_add_u32 v66, v66, 2, v249
	ds_read_b32 v253, v66
	s_or_b64 exec, exec, s[0:1]
	v_mov_b32_e32 v84, 0
	v_mov_b32_e32 v85, 0
	v_mov_b32_e32 v82, 0
	v_mov_b32_e32 v83, 0
	s_and_saveexec_b64 s[0:1], s[8:9]
	s_cbranch_execnz .LBB0_453
	s_or_b64 exec, exec, s[0:1]
	s_and_saveexec_b64 s[0:1], s[4:5]
	s_cbranch_execnz .LBB0_454

.Lvf_wave0:
	s_and_saveexec_b64 s[6:7], vcc
	s_cbranch_execz .LBB1_2
	v_lshlrev_b32_e32 v2, 2, v0
	ds_read2_b32 v[4:5], v2 offset1:17
	ds_read2_b32 v[6:7], v2 offset0:34 offset1:51
	ds_read2_b32 v[8:9], v2 offset0:68 offset1:85
	ds_read2_b32 v[10:11], v2 offset0:102 offset1:119
	ds_read2_b32 v[12:13], v2 offset0:136 offset1:153
	s_waitcnt lgkmcnt(4)
	v_add_u32_e32 v1, v5, v4
	s_waitcnt lgkmcnt(3)
	v_add3_u32 v1, v6, v1, v7
	s_waitcnt lgkmcnt(2)
	v_add3_u32 v1, v8, v1, v9
	ds_read2_b32 v[4:5], v2 offset0:170 offset1:187
	ds_read2_b32 v[6:7], v2 offset0:204 offset1:221
	ds_read2_b32 v[8:9], v2 offset0:238 offset1:255
	s_waitcnt lgkmcnt(4)
	v_add3_u32 v1, v10, v1, v11
	s_waitcnt lgkmcnt(3)
	v_add3_u32 v1, v12, v1, v13
	s_waitcnt lgkmcnt(2)
	v_add3_u32 v1, v4, v1, v5
	s_waitcnt lgkmcnt(1)
	v_add3_u32 v1, v6, v1, v7
	s_waitcnt lgkmcnt(0)
	v_add3_u32 v1, v8, v1, v9
	v_cvt_f32_u32_e32 v1, v1
	s_add_u32 s4, s8, s4
	s_addc_u32 s5, s9, s5
	v_lshl_add_u64 v[2:3], s[4:5], 0, v[2:3]
	s_mov_b32 s3, 0x2080000
	v_add_co_u32_e32 v2, vcc, s3, v2
	v_mul_f32_e32 v1, 0x37000000, v1
	s_nop 0
	v_addc_co_u32_e32 v3, vcc, 0, v3, vcc
	s_mov_b32 s4, 0xd9d7bdbb
	global_store_dword v[2:3], v1, off offset:8
	v_cvt_f64_f32_e32 v[2:3], v1
	s_mov_b32 s5, 0x3ddb7cdf
	v_add_f64 v[4:5], v[2:3], s[4:5]
	s_mov_b32 s4, 0x55555555
	v_frexp_mant_f64_e32 v[6:7], v[4:5]
	s_mov_b32 s5, 0x3fe55555
	v_cmp_gt_f64_e32 vcc, s[4:5], v[6:7]
	s_mov_b32 s4, 0xbf559e2b
	s_mov_b32 s5, 0x3fc3ab76
	v_cndmask_b32_e64 v8, 0, 1, vcc
	v_ldexp_f64 v[6:7], v[6:7], v8
	v_add_f64 v[8:9], v[6:7], 1.0
	v_rcp_f64_e32 v[10:11], v[8:9]
	v_add_f64 v[14:15], v[8:9], -1.0
	v_add_f64 v[12:13], v[6:7], -1.0
	v_add_f64 v[6:7], v[6:7], -v[14:15]
	v_fma_f64 v[14:15], -v[8:9], v[10:11], 1.0
	v_fmac_f64_e32 v[10:11], v[14:15], v[10:11]
	v_fma_f64 v[14:15], -v[8:9], v[10:11], 1.0
	v_fmac_f64_e32 v[10:11], v[14:15], v[10:11]
	v_mul_f64 v[14:15], v[12:13], v[10:11]
	v_mul_f64 v[16:17], v[8:9], v[14:15]
	v_fma_f64 v[8:9], v[14:15], v[8:9], -v[16:17]
	v_fmac_f64_e32 v[8:9], v[14:15], v[6:7]
	v_add_f64 v[6:7], v[16:17], v[8:9]
	v_add_f64 v[18:19], v[12:13], -v[6:7]
	v_add_f64 v[16:17], v[6:7], -v[16:17]
	v_add_f64 v[12:13], v[12:13], -v[18:19]
	v_add_f64 v[6:7], v[12:13], -v[6:7]
	v_add_f64 v[8:9], v[16:17], -v[8:9]
	v_add_f64 v[6:7], v[8:9], v[6:7]
	v_add_f64 v[6:7], v[18:19], v[6:7]
	v_mul_f64 v[6:7], v[10:11], v[6:7]
	v_add_f64 v[8:9], v[14:15], v[6:7]
	v_add_f64 v[10:11], v[8:9], -v[14:15]
	v_add_f64 v[6:7], v[6:7], -v[10:11]
	v_mul_f64 v[10:11], v[8:9], v[8:9]
	v_mov_b32_e32 v12, 0x6b47b09a
	v_mov_b32_e32 v13, 0x3fc38538
	v_fmac_f64_e32 v[12:13], s[4:5], v[10:11]
	v_mov_b32_e32 v14, 0xd7f4df2e
	v_mov_b32_e32 v15, 0x3fc7474d
	v_fmac_f64_e32 v[14:15], v[10:11], v[12:13]
	v_mov_b32_e32 v12, 0x16291751
	v_mov_b32_e32 v13, 0x3fcc71c0
	v_fmac_f64_e32 v[12:13], v[10:11], v[14:15]
	v_mov_b32_e32 v14, 0x9b27acf1
	v_mov_b32_e32 v15, 0x3fd24924
	v_fmac_f64_e32 v[14:15], v[10:11], v[12:13]
	v_mov_b32_e32 v12, 0x998ef7b6
	v_mov_b32_e32 v13, 0x3fd99999
	v_fmac_f64_e32 v[12:13], v[10:11], v[14:15]
	v_mov_b32_e32 v14, 0x55555780
	v_mov_b32_e32 v15, 0x3fe55555
	v_fmac_f64_e32 v[14:15], v[10:11], v[12:13]
	v_ldexp_f64 v[12:13], v[8:9], 1
	v_mul_f64 v[8:9], v[8:9], v[10:11]
	v_mul_f64 v[8:9], v[8:9], v[14:15]
	v_add_f64 v[10:11], v[12:13], v[8:9]
	v_add_f64 v[12:13], v[10:11], -v[12:13]
	v_ldexp_f64 v[6:7], v[6:7], 1
	v_add_f64 v[8:9], v[8:9], -v[12:13]
	v_add_f64 v[6:7], v[6:7], v[8:9]
	v_frexp_exp_i32_f64_e32 v1, v[4:5]
	v_add_f64 v[8:9], v[10:11], v[6:7]
	v_subbrev_co_u32_e32 v1, vcc, 0, v1, vcc
	v_add_f64 v[10:11], v[8:9], -v[10:11]
	s_mov_b32 s4, 0xfefa39ef
	v_add_f64 v[6:7], v[6:7], -v[10:11]
	v_cvt_f64_i32_e32 v[10:11], v1
	s_mov_b32 s5, 0x3fe62e42
	v_mul_f64 v[12:13], v[10:11], s[4:5]
	v_fma_f64 v[14:15], v[10:11], s[4:5], -v[12:13]
	s_mov_b32 s4, 0x3b39803f
	s_mov_b32 s5, 0x3c7abc9e
	v_fmac_f64_e32 v[14:15], s[4:5], v[10:11]
	v_add_f64 v[10:11], v[12:13], v[14:15]
	v_add_f64 v[12:13], v[10:11], -v[12:13]
	v_add_f64 v[12:13], v[14:15], -v[12:13]
	v_add_f64 v[14:15], v[10:11], v[8:9]
	v_add_f64 v[16:17], v[14:15], -v[10:11]
	v_add_f64 v[18:19], v[14:15], -v[16:17]
	v_add_f64 v[10:11], v[10:11], -v[18:19]
	v_add_f64 v[8:9], v[8:9], -v[16:17]
	v_add_f64 v[8:9], v[8:9], v[10:11]
	v_add_f64 v[10:11], v[12:13], v[6:7]
	v_add_f64 v[16:17], v[10:11], -v[12:13]
	v_add_f64 v[18:19], v[10:11], -v[16:17]
	v_add_f64 v[8:9], v[10:11], v[8:9]
	v_add_f64 v[12:13], v[12:13], -v[18:19]
	v_add_f64 v[6:7], v[6:7], -v[16:17]
	v_add_f64 v[10:11], v[14:15], v[8:9]
	v_add_f64 v[6:7], v[6:7], v[12:13]
	v_add_f64 v[12:13], v[10:11], -v[14:15]
	v_add_f64 v[8:9], v[8:9], -v[12:13]
	s_mov_b32 s4, 0
	v_add_f64 v[6:7], v[6:7], v[8:9]
	s_mov_b32 s5, 0x7ff00000
	v_add_f64 v[6:7], v[10:11], v[6:7]
	v_mov_b32_e32 v1, 0x7ff00000
	v_cmp_neq_f64_e32 vcc, s[4:5], v[4:5]
	v_cmp_neq_f64_e64 s[4:5], 0, v[4:5]
	s_nop 0
	v_cndmask_b32_e32 v1, v1, v7, vcc
	v_mov_b32_e32 v7, 0xfff00000
	s_and_b64 vcc, s[4:5], vcc
	v_cndmask_b32_e64 v5, v7, v1, s[4:5]
	v_cndmask_b32_e32 v4, 0, v6, vcc
	v_mul_f64 v[2:3], v[4:5], v[2:3]
	v_lshlrev_b32_e32 v1, 3, v0
	s_nop 1
	v_mov_b32_dpp v4, v2 row_ror:8 row_mask:0xf bank_mask:0xf
	v_mov_b32_dpp v5, v3 row_ror:8 row_mask:0xf bank_mask:0xf
	v_add_f64 v[2:3], v[2:3], v[4:5]
	s_nop 1
	v_mov_b32_dpp v4, v2 row_ror:4 row_mask:0xf bank_mask:0xf
	v_mov_b32_dpp v5, v3 row_ror:4 row_mask:0xf bank_mask:0xf
	v_add_f64 v[2:3], v[2:3], v[4:5]
	s_nop 1
	v_mov_b32_dpp v4, v2 row_ror:2 row_mask:0xf bank_mask:0xf
	v_mov_b32_dpp v5, v3 row_ror:2 row_mask:0xf bank_mask:0xf
	v_add_f64 v[2:3], v[2:3], v[4:5]
	s_nop 1
	v_mov_b32_dpp v4, v2 row_ror:1 row_mask:0xf bank_mask:0xf
	v_mov_b32_dpp v5, v3 row_ror:1 row_mask:0xf bank_mask:0xf
	v_add_f64 v[2:3], v[2:3], v[4:5]
.LBB1_2:
	s_or_b64 exec, exec, s[6:7]
	v_cmp_eq_u32_e32 vcc, 0, v0
	s_and_saveexec_b64 s[6:7], vcc
	v_mov_b32_e32 v1, 0
	s_mov_b32 s0, 0
	s_mov_b32 s1, 0xc2f00000
	v_mul_f64 v[2:3], v[2:3], s[0:1]
	v_max_f64 v[2:3], v[2:3], 0
	s_mov_b32 s1, 0x43300000
	v_add_f64 v[2:3], v[2:3], s[0:1]
	v_mov_b32_e32 v4, 0x101000
	v_add_u32_e32 v3, 0xbdd00000, v3
	s_nop 0
	global_atomic_add_x2 v[6:7], v4, v[2:3], s[10:11] sc0
	s_barrier
	ds_read_b64 v[18:19], v1 offset:1216
	s_movk_i32 s0, 0xffe9
	s_waitcnt lgkmcnt(0)
	v_ldexp_f64 v[8:9], v[18:19], s0
	s_mov_b32 s0, 0
	s_mov_b32 s1, 0x40240000
	v_mul_f64 v[8:9], v[8:9], s[0:1]
	v_cvt_f32_f64_e32 v16, v[8:9]
	s_waitcnt vmcnt(0)
	v_lshrrev_b32_e32 v5, 24, v7
	v_cmp_eq_u32_e32 vcc, 63, v5
	s_cbranch_vccz .Lvf_end
	v_add_co_u32_e32 v6, vcc, v6, v2
	s_nop 1
	v_addc_co_u32_e32 v7, vcc, v7, v3, vcc
	v_and_b32_e32 v7, 0xffffff, v7
	v_cvt_f64_u32_e32 v[0:1], v7
	v_cvt_f64_u32_e32 v[4:5], v6
	v_ldexp_f64 v[0:1], v[0:1], 32
	v_add_f64 v[0:1], v[0:1], v[4:5]
	s_movk_i32 s0, 0xffd0
	v_ldexp_f64 v[0:1], v[0:1], s0
	v_xor_b32_e32 v1, 0x80000000, v1
	s_mov_b32 s0, 0x652b82fe
	s_mov_b32 s1, 0xbff71547
	v_mul_f64 v[4:5], v[0:1], s[0:1]
	s_mov_b32 s0, 0xfefa39ef
	v_rndne_f64_e32 v[4:5], v[4:5]
	s_mov_b32 s1, 0xbfe62e42
	v_fma_f64 v[6:7], v[4:5], s[0:1], -v[0:1]
	s_mov_b32 s0, 0x3b39803f
	s_mov_b32 s1, 0xbc7abc9e
	v_fmac_f64_e32 v[6:7], s[0:1], v[4:5]
	s_mov_b32 s0, 0x6a5dcb37
	v_mov_b32_e32 v8, 0xfca7ab0c
	v_mov_b32_e32 v9, 0x3e928af3
	s_mov_b32 s1, 0x3e5ade15
	v_fmac_f64_e32 v[8:9], s[0:1], v[6:7]
	v_mov_b32_e32 v10, 0x623fde64
	v_mov_b32_e32 v11, 0x3ec71dee
	v_fmac_f64_e32 v[10:11], v[6:7], v[8:9]
	v_mov_b32_e32 v8, 0x7c89e6b0
	v_mov_b32_e32 v9, 0x3efa0199
	v_fmac_f64_e32 v[8:9], v[6:7], v[10:11]
	v_mov_b32_e32 v10, 0x14761f6e
	v_mov_b32_e32 v11, 0x3f2a01a0
	v_fmac_f64_e32 v[10:11], v[6:7], v[8:9]
	v_mov_b32_e32 v8, 0x1852b7b0
	v_mov_b32_e32 v9, 0x3f56c16c
	v_fmac_f64_e32 v[8:9], v[6:7], v[10:11]
	v_mov_b32_e32 v10, 0x11122322
	v_mov_b32_e32 v11, 0x3f811111
	v_fmac_f64_e32 v[10:11], v[6:7], v[8:9]
	v_mov_b32_e32 v8, 0x555502a1
	v_mov_b32_e32 v9, 0x3fa55555
	v_fmac_f64_e32 v[8:9], v[6:7], v[10:11]
	v_mov_b32_e32 v10, 0x55555511
	v_mov_b32_e32 v11, 0x3fc55555
	v_fmac_f64_e32 v[10:11], v[6:7], v[8:9]
	v_mov_b32_e32 v8, 11
	v_mov_b32_e32 v9, 0x3fe00000
	s_mov_b32 s0, 0
	v_fmac_f64_e32 v[8:9], v[6:7], v[10:11]
	s_mov_b32 s1, 0xc0900000
	v_fma_f64 v[8:9], v[6:7], v[8:9], 1.0
	v_cmp_ngt_f64_e32 vcc, s[0:1], v[0:1]
	s_mov_b32 s0, 0
	v_fma_f64 v[6:7], v[6:7], v[8:9], 1.0
	v_cvt_i32_f64_e32 v4, v[4:5]
	s_mov_b32 s1, 0x4090cc00
	v_ldexp_f64 v[4:5], v[6:7], v4
	v_mov_b32_e32 v6, 0x7ff00000
	v_cmp_nlt_f64_e64 s[0:1], s[0:1], v[0:1]
	v_cndmask_b32_e32 v5, v6, v5, vcc
	s_and_b64 vcc, s[0:1], vcc
	v_cndmask_b32_e64 v1, 0, v5, s[0:1]
	v_cndmask_b32_e32 v0, 0, v4, vcc
	v_cvt_f32_f64_e32 v1, v[0:1]
	v_mov_b32_e32 v0, v16
	v_mov_b32_e32 v2, 0x2080000
	global_store_dwordx2 v2, v[0:1], s[8:9]
